# adds grid barrier: non-leader workgroups poll the cross-XCD generation directly (skips the per-XCD release hop)
# baseline (speedup 1.0000x reference)
; __device__ __forceinline__ unsigned xb_ld(unsigned* p)              { return __hip_atomic_load(p, __ATOMIC_RELAXED, __HIP_MEMORY_SCOPE_AGENT); }
; __device__ __forceinline__ unsigned xb_add(unsigned* p, unsigned v) { return __hip_atomic_fetch_add(p, v, __ATOMIC_RELAXED, __HIP_MEMORY_SCOPE_AGENT); }
; #define XB_SPIN(cond, bar) do { unsigned _sp = 0; while (cond) { __builtin_amdgcn_s_sleep(1); \
;     if ((++_sp & 255u) == 0u) { if (xb_ld(&(bar)[XB_TMO])) break; if (_sp > XB_SPIN_CAP) { atomicAdd(&(bar)[XB_TMO], 1u); break; } } } } while (0)
; __device__ __forceinline__ void xcd_barrier(const XcdBarrier& b) {
;     ...
;         const unsigned old = xb_add(&bar[XB_XSUB(b.x)], 1u);
;         const unsigned gen = old / nloc;
;         if (old + 1u == (gen + 1u) * nloc) {
;             __builtin_amdgcn_fence(__ATOMIC_RELEASE, "agent");
;             asm volatile("s_waitcnt vmcnt(0)" ::: "memory");
;             const unsigned og = xb_add(&bar[XB_TOP], 1u);
;             const unsigned tg = og / nx;
;             if (og + 1u == (tg + 1u) * nx) xb_add(&bar[XB_TOPGEN], 1u);
;             else XB_SPIN(xb_ld(&bar[XB_TOPGEN]) == tg, bar);
;             __builtin_amdgcn_fence(__ATOMIC_ACQUIRE, "agent");
;             xb_add(&bar[XB_XGEN(b.x)], 1u);
;             asm volatile("s_waitcnt vmcnt(0)" ::: "memory");
;         } else {
;             XB_SPIN(xb_ld(&bar[XB_XGEN(b.x)]) == gen, bar);
;             __builtin_amdgcn_fence(__ATOMIC_ACQUIRE, "agent");
;             asm volatile("s_waitcnt vmcnt(0)" ::: "memory");
;         }
.LBB0_76:
	s_or_b64 exec, exec, s[44:45]
	v_cvt_f32_u32_e32 v6, v4
	s_waitcnt vmcnt(0)
	v_readfirstlane_b32 s0, v5
	v_sub_u32_e32 v5, 0, v4
	v_rcp_iflag_f32_e32 v6, v6
	v_add_u32_e32 v7, s0, v3
	v_mul_f32_e32 v6, 0x4f7ffffe, v6
	v_cvt_u32_f32_e32 v6, v6
	v_mul_lo_u32 v3, v5, v6
	v_mul_hi_u32 v3, v6, v3
	v_add_u32_e32 v3, v6, v3
	v_mul_hi_u32 v3, v7, v3
	v_mul_lo_u32 v5, v3, v4
	v_sub_u32_e32 v5, v7, v5
	v_add_u32_e32 v6, 1, v3
	v_cmp_ge_u32_e32 vcc, v5, v4
	s_nop 1
	v_cndmask_b32_e32 v3, v3, v6, vcc
	v_sub_u32_e32 v6, v5, v4
	v_cndmask_b32_e32 v5, v5, v6, vcc
	v_add_u32_e32 v6, 1, v3
	v_cmp_ge_u32_e32 vcc, v5, v4
	v_add_u32_e32 v5, 1, v7
	s_nop 0
	v_cndmask_b32_e32 v3, v3, v6, vcc
	v_mul_lo_u32 v6, v4, v3
	v_add_u32_e32 v4, v6, v4
	v_cmp_ne_u32_e32 vcc, v5, v4
	s_and_saveexec_b64 s[0:1], vcc
	s_xor_b64 s[42:43], exec, s[0:1]
	s_cbranch_execz .LBB0_90
	s_waitcnt lgkmcnt(0)
	v_mov_b32_e32 v2, 0x7000
	global_load_dword v2, v2, s[30:31] offset:1280 sc1
	s_add_u32 s54, s30, 0x7500
	s_addc_u32 s55, s31, 0
	s_waitcnt vmcnt(0)
	v_cmp_eq_u32_e32 vcc, v2, v3
	s_and_saveexec_b64 s[44:45], vcc
	s_cbranch_execz .LBB0_89
	s_add_u32 s46, s30, 0x4200
	s_addc_u32 s47, s31, 0
	s_mov_b32 s0, 1
	s_mov_b64 s[56:57], 0
	v_mov_b32_e32 v2, 0
	s_branch .LBB0_80

; __device__ __forceinline__ unsigned xb_ld(unsigned* p)              { return __hip_atomic_load(p, __ATOMIC_RELAXED, __HIP_MEMORY_SCOPE_AGENT); }
; __device__ __forceinline__ unsigned xb_add(unsigned* p, unsigned v) { return __hip_atomic_fetch_add(p, v, __ATOMIC_RELAXED, __HIP_MEMORY_SCOPE_AGENT); }
; #define XB_SPIN(cond, bar) do { unsigned _sp = 0; while (cond) { __builtin_amdgcn_s_sleep(1); \
;     if ((++_sp & 255u) == 0u) { if (xb_ld(&(bar)[XB_TMO])) break; if (_sp > XB_SPIN_CAP) { atomicAdd(&(bar)[XB_TMO], 1u); break; } } } } while (0)
; __device__ __forceinline__ void xcd_barrier(const XcdBarrier& b) {
;     ...
;         const unsigned old = xb_add(&bar[XB_XSUB(b.x)], 1u);
;         const unsigned gen = old / nloc;
;         if (old + 1u == (gen + 1u) * nloc) {
;             __builtin_amdgcn_fence(__ATOMIC_RELEASE, "agent");
;             asm volatile("s_waitcnt vmcnt(0)" ::: "memory");
;             const unsigned og = xb_add(&bar[XB_TOP], 1u);
;             const unsigned tg = og / nx;
;             if (og + 1u == (tg + 1u) * nx) xb_add(&bar[XB_TOPGEN], 1u);
;             else XB_SPIN(xb_ld(&bar[XB_TOPGEN]) == tg, bar);
;             __builtin_amdgcn_fence(__ATOMIC_ACQUIRE, "agent");
;             xb_add(&bar[XB_XGEN(b.x)], 1u);
;             asm volatile("s_waitcnt vmcnt(0)" ::: "memory");
;         } else {
;             XB_SPIN(xb_ld(&bar[XB_XGEN(b.x)]) == gen, bar);
;             __builtin_amdgcn_fence(__ATOMIC_ACQUIRE, "agent");
;             asm volatile("s_waitcnt vmcnt(0)" ::: "memory");
;         }
.LBB0_623:
	s_or_b64 exec, exec, s[18:19]
	v_cvt_f32_u32_e32 v6, v4
	s_waitcnt vmcnt(0)
	v_readfirstlane_b32 s0, v5
	v_sub_u32_e32 v5, 0, v4
	v_rcp_iflag_f32_e32 v6, v6
	v_add_u32_e32 v7, s0, v3
	v_mul_f32_e32 v6, 0x4f7ffffe, v6
	v_cvt_u32_f32_e32 v6, v6
	v_mul_lo_u32 v3, v5, v6
	v_mul_hi_u32 v3, v6, v3
	v_add_u32_e32 v3, v6, v3
	v_mul_hi_u32 v3, v7, v3
	v_mul_lo_u32 v5, v3, v4
	v_sub_u32_e32 v5, v7, v5
	v_add_u32_e32 v6, 1, v3
	v_cmp_ge_u32_e32 vcc, v5, v4
	s_nop 1
	v_cndmask_b32_e32 v3, v3, v6, vcc
	v_sub_u32_e32 v6, v5, v4
	v_cndmask_b32_e32 v5, v5, v6, vcc
	v_add_u32_e32 v6, 1, v3
	v_cmp_ge_u32_e32 vcc, v5, v4
	v_add_u32_e32 v5, 1, v7
	s_nop 0
	v_cndmask_b32_e32 v3, v3, v6, vcc
	v_mul_lo_u32 v6, v4, v3
	v_add_u32_e32 v4, v6, v4
	v_cmp_ne_u32_e32 vcc, v5, v4
	s_and_saveexec_b64 s[0:1], vcc
	s_xor_b64 s[14:15], exec, s[0:1]
	s_cbranch_execz .LBB0_637
	s_waitcnt lgkmcnt(0)
	v_mov_b32_e32 v2, 0x7000
	global_load_dword v2, v2, s[30:31] offset:1280 sc1
	s_add_u32 s42, s30, 0x7500
	s_addc_u32 s43, s31, 0
	s_waitcnt vmcnt(0)
	v_cmp_eq_u32_e32 vcc, v2, v3
	s_and_saveexec_b64 s[18:19], vcc
	s_cbranch_execz .LBB0_636
	s_add_u32 s22, s30, 0x4200
	s_addc_u32 s23, s31, 0
	s_mov_b32 s0, 1
	s_mov_b64 s[44:45], 0
	v_mov_b32_e32 v2, 0
	s_branch .LBB0_627

; __device__ __forceinline__ unsigned xb_ld(unsigned* p)              { return __hip_atomic_load(p, __ATOMIC_RELAXED, __HIP_MEMORY_SCOPE_AGENT); }
; __device__ __forceinline__ unsigned xb_add(unsigned* p, unsigned v) { return __hip_atomic_fetch_add(p, v, __ATOMIC_RELAXED, __HIP_MEMORY_SCOPE_AGENT); }
; #define XB_SPIN(cond, bar) do { unsigned _sp = 0; while (cond) { __builtin_amdgcn_s_sleep(1); \
;     if ((++_sp & 255u) == 0u) { if (xb_ld(&(bar)[XB_TMO])) break; if (_sp > XB_SPIN_CAP) { atomicAdd(&(bar)[XB_TMO], 1u); break; } } } } while (0)
; __device__ __forceinline__ void xcd_barrier(const XcdBarrier& b) {
;     ...
;         const unsigned old = xb_add(&bar[XB_XSUB(b.x)], 1u);
;         const unsigned gen = old / nloc;
;         if (old + 1u == (gen + 1u) * nloc) {
;             __builtin_amdgcn_fence(__ATOMIC_RELEASE, "agent");
;             asm volatile("s_waitcnt vmcnt(0)" ::: "memory");
;             const unsigned og = xb_add(&bar[XB_TOP], 1u);
;             const unsigned tg = og / nx;
;             if (og + 1u == (tg + 1u) * nx) xb_add(&bar[XB_TOPGEN], 1u);
;             else XB_SPIN(xb_ld(&bar[XB_TOPGEN]) == tg, bar);
;             __builtin_amdgcn_fence(__ATOMIC_ACQUIRE, "agent");
;             xb_add(&bar[XB_XGEN(b.x)], 1u);
;             asm volatile("s_waitcnt vmcnt(0)" ::: "memory");
;         } else {
;             XB_SPIN(xb_ld(&bar[XB_XGEN(b.x)]) == gen, bar);
;             __builtin_amdgcn_fence(__ATOMIC_ACQUIRE, "agent");
;             asm volatile("s_waitcnt vmcnt(0)" ::: "memory");
;         }
.LBB0_681:
	s_or_b64 exec, exec, s[18:19]
	v_cvt_f32_u32_e32 v6, v4
	s_waitcnt vmcnt(0)
	v_readfirstlane_b32 s0, v5
	v_sub_u32_e32 v5, 0, v4
	v_rcp_iflag_f32_e32 v6, v6
	v_add_u32_e32 v7, s0, v3
	v_mul_f32_e32 v6, 0x4f7ffffe, v6
	v_cvt_u32_f32_e32 v6, v6
	v_mul_lo_u32 v3, v5, v6
	v_mul_hi_u32 v3, v6, v3
	v_add_u32_e32 v3, v6, v3
	v_mul_hi_u32 v3, v7, v3
	v_mul_lo_u32 v5, v3, v4
	v_sub_u32_e32 v5, v7, v5
	v_add_u32_e32 v6, 1, v3
	v_cmp_ge_u32_e32 vcc, v5, v4
	s_nop 1
	v_cndmask_b32_e32 v3, v3, v6, vcc
	v_sub_u32_e32 v6, v5, v4
	v_cndmask_b32_e32 v5, v5, v6, vcc
	v_add_u32_e32 v6, 1, v3
	v_cmp_ge_u32_e32 vcc, v5, v4
	v_add_u32_e32 v5, 1, v7
	s_nop 0
	v_cndmask_b32_e32 v3, v3, v6, vcc
	v_mul_lo_u32 v6, v4, v3
	v_add_u32_e32 v4, v6, v4
	v_cmp_ne_u32_e32 vcc, v5, v4
	s_and_saveexec_b64 s[0:1], vcc
	s_xor_b64 s[14:15], exec, s[0:1]
	s_cbranch_execz .LBB0_695
	s_waitcnt lgkmcnt(0)
	v_mov_b32_e32 v2, 0x7000
	global_load_dword v2, v2, s[30:31] offset:1280 sc1
	s_add_u32 s36, s30, 0x7500
	s_addc_u32 s37, s31, 0
	s_waitcnt vmcnt(0)
	v_cmp_eq_u32_e32 vcc, v2, v3
	s_and_saveexec_b64 s[18:19], vcc
	s_cbranch_execz .LBB0_694
	s_add_u32 s22, s30, 0x4200
	s_addc_u32 s23, s31, 0
	s_mov_b32 s0, 1
	s_mov_b64 s[38:39], 0
	v_mov_b32_e32 v2, 0
	s_branch .LBB0_685

; __device__ __forceinline__ unsigned xb_ld(unsigned* p)              { return __hip_atomic_load(p, __ATOMIC_RELAXED, __HIP_MEMORY_SCOPE_AGENT); }
; __device__ __forceinline__ unsigned xb_add(unsigned* p, unsigned v) { return __hip_atomic_fetch_add(p, v, __ATOMIC_RELAXED, __HIP_MEMORY_SCOPE_AGENT); }
; #define XB_SPIN(cond, bar) do { unsigned _sp = 0; while (cond) { __builtin_amdgcn_s_sleep(1); \
;     if ((++_sp & 255u) == 0u) { if (xb_ld(&(bar)[XB_TMO])) break; if (_sp > XB_SPIN_CAP) { atomicAdd(&(bar)[XB_TMO], 1u); break; } } } } while (0)
; __device__ __forceinline__ void xcd_barrier(const XcdBarrier& b) {
;     ...
;         const unsigned old = xb_add(&bar[XB_XSUB(b.x)], 1u);
;         const unsigned gen = old / nloc;
;         if (old + 1u == (gen + 1u) * nloc) {
;             __builtin_amdgcn_fence(__ATOMIC_RELEASE, "agent");
;             asm volatile("s_waitcnt vmcnt(0)" ::: "memory");
;             const unsigned og = xb_add(&bar[XB_TOP], 1u);
;             const unsigned tg = og / nx;
;             if (og + 1u == (tg + 1u) * nx) xb_add(&bar[XB_TOPGEN], 1u);
;             else XB_SPIN(xb_ld(&bar[XB_TOPGEN]) == tg, bar);
;             __builtin_amdgcn_fence(__ATOMIC_ACQUIRE, "agent");
;             xb_add(&bar[XB_XGEN(b.x)], 1u);
;             asm volatile("s_waitcnt vmcnt(0)" ::: "memory");
;         } else {
;             XB_SPIN(xb_ld(&bar[XB_XGEN(b.x)]) == gen, bar);
;             __builtin_amdgcn_fence(__ATOMIC_ACQUIRE, "agent");
;             asm volatile("s_waitcnt vmcnt(0)" ::: "memory");
;         }
.LBB0_927:
	s_or_b64 exec, exec, s[14:15]
	v_cvt_f32_u32_e32 v6, v4
	s_waitcnt vmcnt(0)
	v_readfirstlane_b32 s0, v5
	v_sub_u32_e32 v5, 0, v4
	v_rcp_iflag_f32_e32 v6, v6
	v_add_u32_e32 v7, s0, v3
	v_mul_f32_e32 v6, 0x4f7ffffe, v6
	v_cvt_u32_f32_e32 v6, v6
	v_mul_lo_u32 v3, v5, v6
	v_mul_hi_u32 v3, v6, v3
	v_add_u32_e32 v3, v6, v3
	v_mul_hi_u32 v3, v7, v3
	v_mul_lo_u32 v5, v3, v4
	v_sub_u32_e32 v5, v7, v5
	v_add_u32_e32 v6, 1, v3
	v_cmp_ge_u32_e32 vcc, v5, v4
	s_nop 1
	v_cndmask_b32_e32 v3, v3, v6, vcc
	v_sub_u32_e32 v6, v5, v4
	v_cndmask_b32_e32 v5, v5, v6, vcc
	v_add_u32_e32 v6, 1, v3
	v_cmp_ge_u32_e32 vcc, v5, v4
	v_add_u32_e32 v5, 1, v7
	s_nop 0
	v_cndmask_b32_e32 v3, v3, v6, vcc
	v_mul_lo_u32 v6, v4, v3
	v_add_u32_e32 v4, v6, v4
	v_cmp_ne_u32_e32 vcc, v5, v4
	s_and_saveexec_b64 s[0:1], vcc
	s_xor_b64 s[12:13], exec, s[0:1]
	s_cbranch_execz .LBB0_941
	s_waitcnt lgkmcnt(0)
	v_mov_b32_e32 v2, 0x7000
	global_load_dword v2, v2, s[30:31] offset:1280 sc1
	s_add_u32 s22, s30, 0x7500
	s_addc_u32 s23, s31, 0
	s_waitcnt vmcnt(0)
	v_cmp_eq_u32_e32 vcc, v2, v3
	s_and_saveexec_b64 s[14:15], vcc
	s_cbranch_execz .LBB0_940
	s_add_u32 s18, s30, 0x4200
	s_addc_u32 s19, s31, 0
	s_mov_b32 s0, 1
	s_mov_b64 s[36:37], 0
	v_mov_b32_e32 v2, 0
	s_branch .LBB0_931

; __device__ __forceinline__ unsigned xb_ld(unsigned* p)              { return __hip_atomic_load(p, __ATOMIC_RELAXED, __HIP_MEMORY_SCOPE_AGENT); }
; __device__ __forceinline__ unsigned xb_add(unsigned* p, unsigned v) { return __hip_atomic_fetch_add(p, v, __ATOMIC_RELAXED, __HIP_MEMORY_SCOPE_AGENT); }
; #define XB_SPIN(cond, bar) do { unsigned _sp = 0; while (cond) { __builtin_amdgcn_s_sleep(1); \
;     if ((++_sp & 255u) == 0u) { if (xb_ld(&(bar)[XB_TMO])) break; if (_sp > XB_SPIN_CAP) { atomicAdd(&(bar)[XB_TMO], 1u); break; } } } } while (0)
; __device__ __forceinline__ void xcd_barrier(const XcdBarrier& b) {
;     ...
;         const unsigned old = xb_add(&bar[XB_XSUB(b.x)], 1u);
;         const unsigned gen = old / nloc;
;         if (old + 1u == (gen + 1u) * nloc) {
;             __builtin_amdgcn_fence(__ATOMIC_RELEASE, "agent");
;             asm volatile("s_waitcnt vmcnt(0)" ::: "memory");
;             const unsigned og = xb_add(&bar[XB_TOP], 1u);
;             const unsigned tg = og / nx;
;             if (og + 1u == (tg + 1u) * nx) xb_add(&bar[XB_TOPGEN], 1u);
;             else XB_SPIN(xb_ld(&bar[XB_TOPGEN]) == tg, bar);
;             __builtin_amdgcn_fence(__ATOMIC_ACQUIRE, "agent");
;             xb_add(&bar[XB_XGEN(b.x)], 1u);
;             asm volatile("s_waitcnt vmcnt(0)" ::: "memory");
;         } else {
;             XB_SPIN(xb_ld(&bar[XB_XGEN(b.x)]) == gen, bar);
;             __builtin_amdgcn_fence(__ATOMIC_ACQUIRE, "agent");
;             asm volatile("s_waitcnt vmcnt(0)" ::: "memory");
;         }
.LBB0_1022:
	s_or_b64 exec, exec, s[14:15]
	v_cvt_f32_u32_e32 v6, v4
	s_waitcnt vmcnt(0)
	v_readfirstlane_b32 s0, v5
	v_sub_u32_e32 v5, 0, v4
	v_rcp_iflag_f32_e32 v6, v6
	v_add_u32_e32 v7, s0, v3
	v_mul_f32_e32 v6, 0x4f7ffffe, v6
	v_cvt_u32_f32_e32 v6, v6
	v_mul_lo_u32 v3, v5, v6
	v_mul_hi_u32 v3, v6, v3
	v_add_u32_e32 v3, v6, v3
	v_mul_hi_u32 v3, v7, v3
	v_mul_lo_u32 v5, v3, v4
	v_sub_u32_e32 v5, v7, v5
	v_add_u32_e32 v6, 1, v3
	v_cmp_ge_u32_e32 vcc, v5, v4
	s_nop 1
	v_cndmask_b32_e32 v3, v3, v6, vcc
	v_sub_u32_e32 v6, v5, v4
	v_cndmask_b32_e32 v5, v5, v6, vcc
	v_add_u32_e32 v6, 1, v3
	v_cmp_ge_u32_e32 vcc, v5, v4
	v_add_u32_e32 v5, 1, v7
	s_nop 0
	v_cndmask_b32_e32 v3, v3, v6, vcc
	v_mul_lo_u32 v6, v4, v3
	v_add_u32_e32 v4, v6, v4
	v_cmp_ne_u32_e32 vcc, v5, v4
	s_and_saveexec_b64 s[0:1], vcc
	s_xor_b64 s[12:13], exec, s[0:1]
	s_cbranch_execz .LBB0_1036
	s_waitcnt lgkmcnt(0)
	v_mov_b32_e32 v2, 0x7000
	global_load_dword v2, v2, s[30:31] offset:1280 sc1
	s_add_u32 s18, s30, 0x7500
	s_addc_u32 s19, s31, 0
	s_waitcnt vmcnt(0)
	v_cmp_eq_u32_e32 vcc, v2, v3
	s_and_saveexec_b64 s[14:15], vcc
	s_cbranch_execz .LBB0_1035
	s_add_u32 s16, s30, 0x4200
	s_addc_u32 s17, s31, 0
	s_mov_b32 s0, 1
	s_mov_b64 s[20:21], 0
	v_mov_b32_e32 v2, 0
	s_branch .LBB0_1026

; __device__ __forceinline__ unsigned xb_ld(unsigned* p)              { return __hip_atomic_load(p, __ATOMIC_RELAXED, __HIP_MEMORY_SCOPE_AGENT); }
; __device__ __forceinline__ unsigned xb_add(unsigned* p, unsigned v) { return __hip_atomic_fetch_add(p, v, __ATOMIC_RELAXED, __HIP_MEMORY_SCOPE_AGENT); }
; #define XB_SPIN(cond, bar) do { unsigned _sp = 0; while (cond) { __builtin_amdgcn_s_sleep(1); \
;     if ((++_sp & 255u) == 0u) { if (xb_ld(&(bar)[XB_TMO])) break; if (_sp > XB_SPIN_CAP) { atomicAdd(&(bar)[XB_TMO], 1u); break; } } } } while (0)
; __device__ __forceinline__ void xcd_barrier(const XcdBarrier& b) {
;     ...
;         const unsigned old = xb_add(&bar[XB_XSUB(b.x)], 1u);
;         const unsigned gen = old / nloc;
;         if (old + 1u == (gen + 1u) * nloc) {
;             __builtin_amdgcn_fence(__ATOMIC_RELEASE, "agent");
;             asm volatile("s_waitcnt vmcnt(0)" ::: "memory");
;             const unsigned og = xb_add(&bar[XB_TOP], 1u);
;             const unsigned tg = og / nx;
;             if (og + 1u == (tg + 1u) * nx) xb_add(&bar[XB_TOPGEN], 1u);
;             else XB_SPIN(xb_ld(&bar[XB_TOPGEN]) == tg, bar);
;             __builtin_amdgcn_fence(__ATOMIC_ACQUIRE, "agent");
;             xb_add(&bar[XB_XGEN(b.x)], 1u);
;             asm volatile("s_waitcnt vmcnt(0)" ::: "memory");
;         } else {
;             XB_SPIN(xb_ld(&bar[XB_XGEN(b.x)]) == gen, bar);
;             __builtin_amdgcn_fence(__ATOMIC_ACQUIRE, "agent");
;             asm volatile("s_waitcnt vmcnt(0)" ::: "memory");
;         }
.LBB0_1107:
	s_or_b64 exec, exec, s[8:9]
	v_cvt_f32_u32_e32 v6, v4
	s_waitcnt vmcnt(0)
	v_readfirstlane_b32 s6, v5
	v_sub_u32_e32 v5, 0, v4
	v_rcp_iflag_f32_e32 v6, v6
	v_add_u32_e32 v7, s6, v3
	v_mul_f32_e32 v6, 0x4f7ffffe, v6
	v_cvt_u32_f32_e32 v6, v6
	v_mul_lo_u32 v3, v5, v6
	v_mul_hi_u32 v3, v6, v3
	v_add_u32_e32 v3, v6, v3
	v_mul_hi_u32 v3, v7, v3
	v_mul_lo_u32 v5, v3, v4
	v_sub_u32_e32 v5, v7, v5
	v_add_u32_e32 v6, 1, v3
	v_cmp_ge_u32_e32 vcc, v5, v4
	s_nop 1
	v_cndmask_b32_e32 v3, v3, v6, vcc
	v_sub_u32_e32 v6, v5, v4
	v_cndmask_b32_e32 v5, v5, v6, vcc
	v_add_u32_e32 v6, 1, v3
	v_cmp_ge_u32_e32 vcc, v5, v4
	v_add_u32_e32 v5, 1, v7
	s_nop 0
	v_cndmask_b32_e32 v3, v3, v6, vcc
	v_mul_lo_u32 v6, v4, v3
	v_add_u32_e32 v4, v6, v4
	v_cmp_ne_u32_e32 vcc, v5, v4
	s_and_saveexec_b64 s[6:7], vcc
	s_xor_b64 s[6:7], exec, s[6:7]
	s_cbranch_execz .LBB0_1121
	s_waitcnt lgkmcnt(0)
	v_mov_b32_e32 v2, 0x7000
	global_load_dword v2, v2, s[30:31] offset:1280 sc1
	s_add_u32 s14, s30, 0x7500
	s_addc_u32 s15, s31, 0
	s_waitcnt vmcnt(0)
	v_cmp_eq_u32_e32 vcc, v2, v3
	s_and_saveexec_b64 s[8:9], vcc
	s_cbranch_execz .LBB0_1120
	s_add_u32 s12, s30, 0x4200
	s_addc_u32 s13, s31, 0
	s_mov_b32 s10, 1
	s_mov_b64 s[16:17], 0
	v_mov_b32_e32 v2, 0
	s_branch .LBB0_1111
